# in-proj and gates GEMM: next-unit rstd partial loads issued one K-loop trip earlier into dead VGPRs, removing the vmcnt(0) drain inside the K-loop; gates bias loads moved to last trip
# speedup vs baseline: 1.0171x; 1.0004x over previous
.LBB0_227:
	s_cmp_eq_u32 s53, 10
	s_cselect_b64 s[28:29], -1, 0
	s_and_b64 s[30:31], s[24:25], s[28:29]
	s_andn2_b64 vcc, exec, s[30:31]
	s_cbranch_vccnz .Lmy_ar_ip_skip
	s_movk_i32 s30, 0x100
	v_cmp_gt_i32_e32 vcc, s30, v0
	s_and_saveexec_b64 s[30:31], vcc
	s_cbranch_execz .Lmy_ar_ip_rest
	v_add_u32_e32 v132, s15, v0
	v_ashrrev_i32_e32 v133, 31, v132
	v_lshlrev_b64 v[132:133], 6, v[132:133]
	v_lshl_add_u64 v[144:145], s[10:11], 0, v[132:133]
	global_load_dwordx4 v[236:239], v[144:145], off offset:48
	global_load_dwordx4 v[240:243], v[144:145], off offset:32
	global_load_dwordx4 v[244:247], v[144:145], off offset:16
	global_load_dwordx4 v[248:251], v[144:145], off

.Lmy_ar_ip_skip:
	s_cmp_eq_u32 s53, 12
	s_cselect_b64 s[28:29], -1, 0
	s_and_b64 s[30:31], s[24:25], s[28:29]
	s_andn2_b64 vcc, exec, s[30:31]
	s_cbranch_vccnz .LBB0_226
	v_mov_b32_e32 v2, v0
	s_movk_i32 s30, 0x100
	s_nop 0
	v_cmp_gt_i32_e32 vcc, s30, v2
	s_and_saveexec_b64 s[30:31], vcc
	s_cbranch_execz .LBB0_225
	v_lshl_add_u32 v2, v2, 2, s17
	v_mov_b32_e32 v132, v236
	v_mov_b32_e32 v133, v237
	v_mov_b32_e32 v134, v238
	v_mov_b32_e32 v135, v239
	v_mov_b32_e32 v136, v240
	v_mov_b32_e32 v137, v241
	v_mov_b32_e32 v138, v242
	v_mov_b32_e32 v139, v243
	v_mov_b32_e32 v140, v244
	v_mov_b32_e32 v141, v245
	v_mov_b32_e32 v142, v246
	v_mov_b32_e32 v143, v247
	v_mov_b32_e32 v144, v248
	v_mov_b32_e32 v145, v249
	v_mov_b32_e32 v146, v250
	v_mov_b32_e32 v147, v251
	v_add_f32_e32 v136, v136, v137
	v_add_f32_e32 v138, v138, v139
	v_mov_b32_e32 v160, v145
	v_mov_b32_e32 v161, v146
	v_mov_b32_e32 v145, v147
	v_mov_b32_e32 v146, v141
	v_mov_b32_e32 v147, v142
	v_mov_b32_e32 v141, v143
	v_pk_add_f32 v[144:145], v[160:161], v[144:145]
	v_pk_add_f32 v[140:141], v[146:147], v[140:141]
	v_pk_add_f32 v[144:145], v[144:145], v[144:145] op_sel:[0,1] op_sel_hi:[1,0]
	v_pk_add_f32 v[140:141], v[140:141], v[140:141] op_sel:[0,1] op_sel_hi:[1,0]
	v_mov_b32_e32 v145, v132
	v_mov_b32_e32 v141, v133
	v_mov_b32_e32 v137, v134
	v_mov_b32_e32 v139, v135
	v_pk_add_f32 v[132:133], v[144:145], v[140:141]
	v_pk_add_f32 v[134:135], v[136:137], v[138:139]
	s_nop 0
	v_pk_add_f32 v[132:133], v[132:133], v[134:135]
	s_nop 0
	v_add_f32_e32 v132, v132, v133
	v_fmamk_f32 v132, v132, 0x3a800000, v1
	v_cmp_gt_f32_e32 vcc, s85, v132
	v_mul_f32_e32 v133, 0x4b800000, v132
	s_nop 0
	v_cndmask_b32_e32 v132, v132, v133, vcc
	v_rsq_f32_e32 v132, v132
	s_nop 0
	v_mul_f32_e32 v133, 0x45800000, v132
	v_cndmask_b32_e32 v132, v132, v133, vcc
	ds_write_b32 v2, v132
	s_branch .LBB0_225

.LBB0_1977:
	s_cmp_lg_u32 s64, 12
	s_cbranch_scc1 .Lmy_bias_skip
	s_lshl_b32 s100, s19, 8
	s_add_i32 s100, s100, 0xffffee00
	s_lshl_b32 s100, s100, 2
	s_add_u32 s100, s54, s100
	s_addc_u32 s101, s55, 0
	v_bfe_u32 v235, v162, 4, 2
	v_lshlrev_b32_e32 v235, 5, v235
	s_nop 1
	global_load_dwordx4 v[236:239], v235, s[100:101]
	global_load_dwordx4 v[240:243], v235, s[100:101] offset:16
	global_load_dwordx4 v[244:247], v235, s[100:101] offset:512
	global_load_dwordx4 v[248:251], v235, s[100:101] offset:528

.LBB0_1978:
	s_cmp_eq_u32 s64, 10
	s_cselect_b64 s[36:37], -1, 0
	s_and_b64 s[38:39], s[30:31], s[36:37]
	s_andn2_b64 vcc, exec, s[38:39]
	s_cbranch_vccnz .Lmy_ar_g_skip
	s_movk_i32 s38, 0x100
	v_cmp_gt_i32_e32 vcc, s38, v0
	s_and_saveexec_b64 s[38:39], vcc
	s_cbranch_execz .Lmy_ar_g_rest
	v_add_u32_e32 v132, s21, v0
	v_ashrrev_i32_e32 v133, 31, v132
	v_lshlrev_b64 v[132:133], 6, v[132:133]
	v_lshl_add_u64 v[144:145], s[10:11], 0, v[132:133]
	global_load_dwordx4 v[236:239], v[144:145], off offset:48
	global_load_dwordx4 v[240:243], v[144:145], off offset:32
	global_load_dwordx4 v[244:247], v[144:145], off offset:16
	global_load_dwordx4 v[248:251], v[144:145], off

.Lmy_ar_g_skip:
	s_cmp_eq_u32 s64, 12
	s_cselect_b64 s[36:37], -1, 0
	s_and_b64 s[38:39], s[30:31], s[36:37]
	s_andn2_b64 vcc, exec, s[38:39]
	s_cbranch_vccnz .LBB0_1977
	v_mov_b32_e32 v2, v0
	s_movk_i32 s38, 0x100
	s_nop 0
	v_cmp_gt_i32_e32 vcc, s38, v2
	s_and_saveexec_b64 s[38:39], vcc
	s_cbranch_execz .LBB0_1976
	v_lshl_add_u32 v2, v2, 2, s59
	v_mov_b32_e32 v132, v236
	v_mov_b32_e32 v133, v237
	v_mov_b32_e32 v134, v238
	v_mov_b32_e32 v135, v239
	v_mov_b32_e32 v136, v240
	v_mov_b32_e32 v137, v241
	v_mov_b32_e32 v138, v242
	v_mov_b32_e32 v139, v243
	v_mov_b32_e32 v140, v244
	v_mov_b32_e32 v141, v245
	v_mov_b32_e32 v142, v246
	v_mov_b32_e32 v143, v247
	v_mov_b32_e32 v144, v248
	v_mov_b32_e32 v145, v249
	v_mov_b32_e32 v146, v250
	v_mov_b32_e32 v147, v251
	v_add_f32_e32 v136, v136, v137
	v_add_f32_e32 v138, v138, v139
	v_mov_b32_e32 v160, v145
	v_mov_b32_e32 v161, v146
	v_mov_b32_e32 v145, v147
	v_mov_b32_e32 v146, v141
	v_mov_b32_e32 v147, v142
	v_mov_b32_e32 v141, v143
	v_pk_add_f32 v[144:145], v[160:161], v[144:145]
	v_pk_add_f32 v[140:141], v[146:147], v[140:141]
	v_pk_add_f32 v[144:145], v[144:145], v[144:145] op_sel:[0,1] op_sel_hi:[1,0]
	v_pk_add_f32 v[140:141], v[140:141], v[140:141] op_sel:[0,1] op_sel_hi:[1,0]
	v_mov_b32_e32 v145, v132
	v_mov_b32_e32 v141, v133
	v_mov_b32_e32 v137, v134
	v_mov_b32_e32 v139, v135
	v_pk_add_f32 v[132:133], v[144:145], v[140:141]
	v_pk_add_f32 v[134:135], v[136:137], v[138:139]
	s_nop 0
	v_pk_add_f32 v[132:133], v[132:133], v[134:135]
	s_nop 0
	v_add_f32_e32 v132, v132, v133
	v_fmamk_f32 v132, v132, 0x3a800000, v1
	v_cmp_gt_f32_e32 vcc, s85, v132
	v_mul_f32_e32 v133, 0x4b800000, v132
	s_nop 0
	v_cndmask_b32_e32 v132, v132, v133, vcc
	v_rsq_f32_e32 v132, v132
	s_nop 0
	v_mul_f32_e32 v133, 0x45800000, v132
	v_cndmask_b32_e32 v132, v132, v133, vcc
	ds_write_b32 v2, v132
	s_branch .LBB0_1976
